# v47 with the convert-before-attention group chosen as whole XCDs (blockIdx bit 2) so all query blocks of a head run their attention together
# baseline (speedup 1.0000x reference)
;     __device__ __forceinline__ const float* in(int i) const { return *(const float* const __attribute__((address_space(4)))*)(p + 8 * i); }
;     __device__ __forceinline__ unsigned char* ws() const { return *(unsigned char* const __attribute__((address_space(4)))*)(p + 232); }
; #define SEAM(k) do { if (!MK_PER_PHASE && (k) + 1 < hi) xcd_barrier_work(bar, a, ws, F.lds); } while (0)
; #define PHASE_BEGIN() const KA a = fresh_ka(); unsigned char* ws = a.ws(); Frame F = make_frame(ws); (void)F
; __global__ void __launch_bounds__(512, 2) mk_fwd(Args args) {
;     ...
; #pragma unroll 1
;     for (int l = 0; l < NLAYER; ++l) {
;         const int pb = 2 + 8 * l;
;         if (PT(2) && IN(pb + 0)) {
;             PHASE_BEGIN(); unsigned char* wl = ws + WS_W + (size_t)l * W_LSTRIDE;
;             pg8::DenseSched S; S.init(ws + WS_H, DM, wl + W_IN, NTOK, UW, DM, F.G, (int)blockIdx.x);
;             pg8::EpiBf16 E{(bf16*)(ws + WS_U), UW};
;             pg8::gemm_phase<GEMM_SP2, true>(F.lds, S, E, DM);
;             SEAM(pb + 0);
;         }
;         if (PT(3) && IN(pb + 1)) {
;             PHASE_BEGIN(); bf16* U = (bf16*)(ws + WS_U);
;             const float* gq = a.in(5) + (size_t)l * 512; const float* gkv = a.in(7) + (size_t)l * 256;
;             for (int row = F.gw; row < NTOK; row += F.NGW)
;                 post_u_row(U + (size_t)row * UW, row & (SEQ - 1), gq, gkv, (const f32x2*)(ws + WS_ROPEM), (const f32x2*)(ws + WS_ROPED), F.lane);
;             SEAM(pb + 1);
;         }
;         if (PT(4) && IN(pb + 2)) {
;             PHASE_BEGIN(); unsigned char* wl = ws + WS_W + (size_t)l * W_LSTRIDE; bf16* U = (bf16*)(ws + WS_U);
;             const bool has_na = (((int)blockIdx.x >> 3) & 1) == 0 || F.G != 256;
;             { pg8::DenseSched S;
;               if (F.G == 256) S.init(U + U_CQ, UW, wl + W_UQ, NTOK, QMW, 512, 128, has_na ? (1 << 20) : (int)((blockIdx.x & 7) + 8 * (blockIdx.x >> 4)));
;     ...
;             const bool conv_first = ((blockIdx.x >> 3) & 1) != 0;
;             if (conv_first) conv_drain(a, ws, F.lds, (l + 1) * Q_PER_L, CONV_QUOTA);
;             for (int c = blockIdx.x; c < 256; c += F.G) {
.LBB0_245:
	s_cmpk_lt_i32 s74, 0x200
	s_cselect_b64 s[0:1], -1, 0
	s_lshl_b32 s73, s30, 6
	v_writelane_b32 v254, s0, 0
	s_mov_b32 s69, 0
	s_movk_i32 s75, 0x41
	v_writelane_b32 v254, s1, 1
	s_ashr_i32 s0, s74, 31
	s_lshr_b32 s0, s0, 29
	s_add_i32 s0, s74, s0
	s_ashr_i32 s2, s0, 3
	s_and_b32 s0, s0, -8
	s_sub_i32 s3, s74, s0
	s_lshl_b32 s4, s3, 6
	s_and_b32 s0, s74, 8
	s_bitcmp1_b32 s74, 2
	s_cselect_b64 s[6:7], -1, 0
	v_writelane_b32 v254, s6, 2
	s_lshr_b32 s1, s74, 1
	s_and_b32 s5, s74, 7
	v_writelane_b32 v254, s7, 3
	s_and_b32 s1, s1, 0x7ffffff8
	v_writelane_b32 v254, s5, 4
	s_or_b32 s5, s1, s5
	s_cmp_eq_u32 s0, 0
	s_cselect_b64 s[0:1], -1, 0
	v_writelane_b32 v254, s0, 5
	s_movk_i32 s58, 0xc0
	s_movk_i32 s59, 0x80
	v_writelane_b32 v254, s1, 6
	s_and_b64 s[0:1], s[0:1], exec
	s_cselect_b32 s0, 0x100000, s5
	s_cmpk_lt_i32 s74, 0x100
	v_writelane_b32 v254, s0, 7
	s_cselect_b64 s[88:89], -1, 0
	s_lshl_b32 s0, s3, 5
	s_lshr_b32 s1, s74, 3
	v_writelane_b32 v254, s1, 8
	s_cmp_lt_i32 s3, 0
	s_mul_i32 s1, s3, 0x41
	s_mul_i32 s3, s3, 33
	s_cselect_b32 s1, s1, s4
	s_cselect_b32 s3, s3, s0
	s_add_i32 s0, s1, s2
	s_ashr_i32 s1, s0, 31
	s_lshr_b32 s1, s1, 25
	s_add_i32 s1, s0, s1
	s_and_b32 s4, s1, 0xff80
	s_sub_i32 s4, s0, s4
	s_bfe_i32 s0, s4, 0x80000
	s_bfe_u32 s0, s0, 0x3000c
	s_add_i32 s5, s4, s0
	s_bfe_i32 s0, s5, 0x80000
	s_and_b32 s5, s5, 0xf8
	s_sub_i32 s4, s4, s5
	s_sext_i32_i8 s4, s4
	s_lshl_b32 s1, s1, 4
	s_sext_i32_i16 s0, s0
	s_and_b32 s1, s1, 0xfffff800
	s_lshl_b32 s4, s4, 8
	s_lshr_b32 s0, s0, 3
	s_add_i32 s1, s4, s1
	v_writelane_b32 v254, s1, 9
	s_lshl_b32 s1, s0, 8
	v_writelane_b32 v254, s1, 10
	s_bfe_i64 s[0:1], s[0:1], 0x100000
	s_lshl_b64 s[0:1], s[0:1], 20
	v_writelane_b32 v254, s0, 11
	s_add_i32 s91, 0, 0x23f00
	s_mov_b32 s96, 0x10000
	v_writelane_b32 v254, s1, 12
	s_add_i32 s0, s3, s2
	s_ashr_i32 s1, s0, 31
	s_lshr_b32 s1, s1, 26
	s_add_i32 s1, s0, s1
	s_and_b32 s2, s1, 0xffc0
	s_sub_i32 s2, s0, s2
	s_bfe_i32 s0, s2, 0x80000
	s_bfe_u32 s0, s0, 0x3000c
	s_add_i32 s3, s2, s0
	s_bfe_i32 s0, s3, 0x80000
	s_and_b32 s3, s3, 0xf8
	s_sub_i32 s2, s2, s3
	s_sext_i32_i16 s0, s0
	s_sext_i32_i8 s2, s2
	s_lshl_b32 s1, s1, 5
	s_lshr_b32 s0, s0, 3
	s_and_b32 s1, s1, 0xfffff800
	s_lshl_b32 s2, s2, 8
	s_add_i32 s90, s2, s1
	s_lshl_b32 s1, s0, 8
	v_writelane_b32 v254, s1, 13
	s_bfe_i64 s[0:1], s[0:1], 0x100000
	s_lshl_b64 s[2:3], s[0:1], 17
	v_writelane_b32 v254, s2, 14
	s_lshl_b64 s[0:1], s[0:1], 20
	v_mov_b32_e32 v193, 0
	v_writelane_b32 v254, s3, 15
	v_writelane_b32 v254, s0, 16
	s_mov_b32 s3, 0x20000
	s_mov_b32 s2, 0x5800000
	v_writelane_b32 v254, s1, 17
	s_lshl_b32 s0, s74, 4
	v_writelane_b32 v254, s0, 18
	s_lshl_b32 s0, s74, 7
	v_writelane_b32 v254, s0, 19
	s_lshl_b32 s0, s74, 5
	v_writelane_b32 v254, s0, 20
	s_mov_b32 s0, 0x3e4ccccd
	v_writelane_b32 v254, s0, 21
	s_add_i32 s0, 0, 0x23e20
	v_writelane_b32 v254, s0, 22
	s_add_i32 s0, 0, 0x23e24
	v_writelane_b32 v254, s0, 23
	s_add_i32 s0, 0, 0x23e30
	v_writelane_b32 v254, s0, 24
	s_add_i32 s0, 0, 0x23e34
	v_writelane_b32 v254, s0, 25
	s_add_i32 s0, 0, 0x23e3c
	v_writelane_b32 v254, s0, 26
	s_add_i32 s0, 0, 0x23e38
	v_writelane_b32 v254, s0, 27
	s_add_i32 s0, 0, 0x1f000
	v_writelane_b32 v254, s0, 28
	s_add_i32 s0, 0, 0x1e800
	v_writelane_b32 v254, s0, 29
	s_add_i32 s0, 0, 0x20400
	v_writelane_b32 v254, s0, 30
	s_add_i32 s0, 0, 0x22400
	v_writelane_b32 v254, s0, 31
	s_add_i32 s0, 0, 0x22500
	v_writelane_b32 v254, s0, 32
	s_add_i32 s0, 0, 0x20240
	v_writelane_b32 v254, s0, 33
	s_add_i32 s0, 0, 0x20100
	v_writelane_b32 v254, s0, 34
	s_add_i32 s0, 0, 0x20640
	v_writelane_b32 v254, s0, 35
	s_add_i32 s0, 0, 0x20104
	v_writelane_b32 v254, s0, 36
	v_writelane_b32 v254, s0, 37
	s_movk_i32 s60, 0x60
	v_mov_b32_e32 v219, 1
	v_writelane_b32 v254, s1, 38
	v_writelane_b32 v254, s2, 39
	v_writelane_b32 v254, s3, 40
	s_mov_b64 s[0:1], -1
	v_writelane_b32 v254, s0, 41
	s_movk_i32 s61, 0xa0
	s_mov_b32 s93, 0xc3e00000
	v_writelane_b32 v254, s1, 42
	v_writelane_b32 v254, s74, 43
	v_writelane_b32 v254, s76, 44
	v_mov_b32_e32 v218, 0x358637bd
	s_movk_i32 s87, 0xf0
	v_writelane_b32 v254, s77, 45
	v_writelane_b32 v254, s78, 46
	s_movk_i32 s62, 0xe0
	v_mov_b32_e32 v227, 0x3727c5ac
	v_writelane_b32 v254, s79, 47
	v_writelane_b32 v254, s80, 48
	v_mov_b32_e32 v224, 0x43e00000
	v_mov_b32_e32 v220, 0xf149f2ca
	v_writelane_b32 v254, s81, 49
	v_writelane_b32 v254, s82, 50
	v_bfrev_b32_e32 v221, 60
	v_mov_b32_e32 v228, 0xba000000
	v_writelane_b32 v254, s83, 51
	v_writelane_b32 v254, s66, 52
	v_writelane_b32 v254, s73, 53
	v_writelane_b32 v254, s88, 54
	v_mov_b32_e32 v231, 0x3a000000
	v_mov_b32_e32 v222, 0xff800000
	v_writelane_b32 v254, s89, 55
	v_writelane_b32 v254, s90, 56
	s_mov_b64 s[4:5], 0
	s_mov_b64 s[94:95], 0x80
	s_mov_b32 s92, 0x3e38aa3b
	s_mov_b32 s2, s69
	s_mov_b32 s86, 0xb000000
	v_writelane_b32 v254, s91, 57
	s_branch .LBB0_251

; #define LAS __attribute__((address_space(3)))
; __device__ __forceinline__ unsigned xb_ld(unsigned* p)              { return __hip_atomic_load(p, __ATOMIC_RELAXED, __HIP_MEMORY_SCOPE_AGENT); }
; __device__ __forceinline__ unsigned xb_add(unsigned* p, unsigned v) { return __hip_atomic_fetch_add(p, v, __ATOMIC_RELAXED, __HIP_MEMORY_SCOPE_AGENT); }
;     __device__ __forceinline__ unsigned char* ws() const { return *(unsigned char* const __attribute__((address_space(4)))*)(p + 232); }
;     volatile LAS unsigned* st = (volatile LAS unsigned*)(lds + MISC_OFF) + 8;
;     unsigned* qw = (unsigned*)(ws + WS_CTL) + CW_Q;
;     int tl = tid_x(); asm volatile("" : "+v"(tl));
;     const int wave = __builtin_amdgcn_readfirstlane(tl >> 6), lane = tl & 63;
;     LAS float* scr = (LAS float*)(lds + wave * 16640);
;     __syncthreads();
;     unsigned ahead = 0xFFFFFFFFu;
;     if (tl == 0 && max_claims > 0) { if (xb_ld(qw) < (unsigned)target) ahead = xb_add(qw, 32u); }
; __global__ void __launch_bounds__(512, 2) mk_fwd(Args args) {
;     ...
;             const bool conv_first = ((blockIdx.x >> 3) & 1) != 0;
;             if (conv_first) conv_drain(a, ws, F.lds, (l + 1) * Q_PER_L, CONV_QUOTA);
;             for (int c = blockIdx.x; c < 256; c += F.G) {
;                 const int xcd = c & 7, j = c >> 3;
;                 if (ATT_MASK & 1) att::attn_unit<att::MODE_MLA>(P, (xcd * 2 + (j >> 4)) * 16 + (j & 15), al);
;             }
;             if (!conv_first) conv_drain(a, ws, F.lds, (l + 1) * Q_PER_L, CONV_QUOTA);
.LBB0_795:
	v_readlane_b32 s0, v254, 2
	v_readlane_b32 s1, v254, 3
	s_andn2_b64 vcc, exec, s[0:1]
	s_cbranch_vccz .LBB0_887
	v_readlane_b32 s0, v254, 60
	s_mul_i32 s27, s0, 0xc300
	s_add_i32 s25, s27, 0xc300
	s_add_u32 s4, s8, 0x20000
	s_getreg_b32 s0, hwreg(HW_REG_HW_ID, 0, 6)
	s_addc_u32 s5, s9, 0
	s_and_b32 s0, s0, 63
	s_lshl_b32 s0, s0, 2
	s_add_i32 s0, s0, 0
	s_add_i32 s0, s0, 0x23f00
	s_waitcnt vmcnt(15)
	v_mov_b32_e32 v0, s0
	ds_read_b32 v0, v0
	v_mbcnt_lo_u32_b32 v1, -1, 0
	v_mbcnt_hi_u32_b32 v1, -1, v1
	v_readlane_b32 s1, v254, 61
	v_mov_b32_e32 v129, -1
	s_waitcnt lgkmcnt(0)
	v_readfirstlane_b32 s0, v0
	s_nop 1
	v_lshl_add_u32 v0, s0, 6, v1
	s_nop 0
	v_readfirstlane_b32 s14, v0
	v_cmp_eq_u32_e64 s[2:3], 0, v0
	s_barrier
	s_and_saveexec_b64 s[0:1], s[2:3]
	s_cbranch_execz .LBB0_801
	global_load_dword v1, v193, s[4:5] sc1
	v_mov_b32_e32 v129, -1
	s_waitcnt vmcnt(0)
	v_cmp_le_u32_e32 vcc, s25, v1
	s_cbranch_vccnz .LBB0_801
	s_mov_b64 s[12:13], exec
	v_mbcnt_lo_u32_b32 v1, s12, 0
	v_mbcnt_hi_u32_b32 v1, s13, v1
	v_cmp_eq_u32_e32 vcc, 0, v1
	s_and_saveexec_b64 s[10:11], vcc
	s_cbranch_execz .LBB0_800
	s_bcnt1_i32_b64 s12, s[12:13]
	s_lshl_b32 s12, s12, 5
	v_mov_b32_e32 v2, s12
	global_atomic_add v2, v193, v2, s[4:5] sc0
